# softmax exps of both attention tile loops issued behind the P.V MFMAs (8 gqa16 results renamed to v240-247, 4 diff16 results to v240-243); 12 of the 16 gqa16 bf16 packs moved from in front of the barr
# speedup vs baseline: 1.0258x; 1.0112x over previous
; #define HLOADV(kt) do { const char* vb_ = (const char*)Vh + (size_t)(kt) * (64 * LDK * 2); sv0 = *(const bf16x8*)(vb_ + koff0); sv1 = *(const bf16x8*)(vb_ + koff1); } while (0)
; #define HLOADK(kt) do { const char* kb_ = (const char*)Kh + (size_t)(kt) * (64 * LDK * 2); sk0 = *(const bf16x8*)(kb_ + koff0); sk1 = *(const bf16x8*)(kb_ + koff1); } while (0)
; #define HWRITEV(b) do { char* d_ = V_lds + (b) * G16_V; *(bf16x8*)(d_ + vst0) = sv0; *(bf16x8*)(d_ + vst1) = sv1; } while (0)
; #define HWRITEK(b) do { char* d_ = K_lds + (b) * GB_K; *(bf16x8*)(d_ + KSWZ(sr, sc * 2)) = sk0; *(bf16x8*)(d_ + KSWZ(32 + sr, sc * 2)) = sk1; } while (0)
; #define HEXP() do { _Pragma("unroll") for (int kt = 0; kt < 4; ++kt) { _Pragma("unroll") for (int qt = 0; qt < 2; ++qt) { _Pragma("unroll") for (int i = 0; i < 4; ++i) s[kt][qt][i] = __builtin_amdgcn_exp2f(fmaf(s[kt][qt][i], C, mnC)); } } } while (0)
; template <int LDQ, int LDK, int LDO>
; __device__ __forceinline__ void attn_gqa16_body(const bf16* __restrict__ Qb, const bf16* __restrict__ Kh, const bf16* __restrict__ Vh, bf16* __restrict__ Ob, int seq, char* lds, float mref) {
;     ...
;   { int l16q = l16, gq = g, widq = wid; asm volatile("" : "+v"(l16q), "+v"(gq), "+v"(widq));
;     const bf16* Qw = Qb + (widq >> 2) * 128 + (long)((widq & 3) * QBLK + l16q) * LDQ + gq * 8;
; #pragma unroll
;     for (int qt = 0; qt < 2; ++qt)
; #pragma unroll
;       for (int ds = 0; ds < 4; ++ds) qr[qt][ds] = *reinterpret_cast<const bf16x8*>(Qw + (long)qt * 16 * LDQ + ds * 32); }
;   const int sr = tid >> 4, sc = (tid & 15) * 8;
;   const int vst0 = (sc >> 4) * VP16 + sr * 32 + ((sc >> 3) & 1) * 16, vst1 = vst0 + 1024;
;   const int vb0 = (int)(uintptr_t)V_lds + (4 * g + (l16 >> 2)) * 32 + (l16 & 3) * 8;
;   const int kb0 = l16 * 272 + g * 16;
;   bf16x8 sv0, sv1, sk0, sk1;
;   const unsigned koff0 = (unsigned)(sr * LDK + sc) * 2u, koff1 = koff0 + 32u * LDK * 2u;
;     ...
;   f32x4a s[4][2]; bf16x8 pb[2][2];
;     ...
;   const int NT = seq / KVBLK;
;   HLOADK(0); HLOADV(0); asm volatile("s_waitcnt vmcnt(0)" ::: "memory"); HWRITEK(0); HWRITEV(0);
;   HLOADK(1); asm volatile("s_waitcnt vmcnt(0)" ::: "memory"); HWRITEK(1); __syncthreads();
;   HLOADK(2); HLOADV(1);
;   HQK(0); HEXP();
.LBB0_646:
	s_and_b64 vcc, exec, s[14:15]
	s_cbranch_vccz .LBB0_641
	s_lshl_b32 s8, s45, 7
	s_and_b32 s8, s8, 0x3f80
	s_ashr_i32 s14, s45, 8
	s_mul_i32 s12, s8, 0x2400
	s_add_u32 s15, s33, s12
	s_addc_u32 s17, s35, 0
	s_lshl_b32 s13, s45, 1
	s_lshl_b32 s12, s14, 9
	s_and_b32 s13, s13, 0x100
	s_or_b32 s12, s12, s13
	s_ashr_i32 s13, s12, 31
	v_mov_b32_e32 v4, v180
	v_mov_b32_e32 v2, v185
	v_mov_b32_e32 v5, v176
	s_lshl_b64 s[12:13], s[12:13], 1
	s_add_u32 s16, s15, s12
	v_lshlrev_b32_e32 v6, 5, v2
	v_and_b32_e32 v2, 0xffffff80, v6
	s_addc_u32 s17, s17, s13
	v_ashrrev_i32_e32 v3, 31, v2
	v_and_b32_e32 v6, 0x60, v6
	s_lshl_b32 s14, s14, 7
	v_lshl_add_u64 v[2:3], v[2:3], 1, s[16:17]
	v_add_u32_e32 v4, v6, v4
	s_ashr_i32 s15, s14, 31
	v_mad_i64_i32 v[2:3], s[16:17], v4, s26, v[2:3]
	v_lshlrev_b32_e32 v4, 3, v5
	s_lshl_b64 s[46:47], s[14:15], 1
	v_ashrrev_i32_e32 v5, 31, v4
	s_add_u32 s48, s21, s46
	v_lshl_add_u64 v[6:7], v[4:5], 1, v[2:3]
	s_addc_u32 s49, s22, s47
	global_load_dwordx4 v[30:33], v[6:7], off
	global_load_dwordx4 v[18:21], v[6:7], off offset:64
	global_load_dwordx4 v[10:13], v[6:7], off offset:128
	global_load_dwordx4 v[2:5], v[6:7], off offset:192
	v_add_co_u32_e32 v6, vcc, s27, v6
	s_add_u32 s46, s23, s46
	s_nop 0
	v_addc_co_u32_e32 v7, vcc, 0, v7, vcc
	v_lshl_add_u64 v[102:103], s[48:49], 0, v[178:179]
	s_addc_u32 s47, s24, s47
	s_add_u32 s74, s46, 0x90000
	s_addc_u32 s75, s47, 0
	s_add_u32 s76, s74, 0x48000
	s_addc_u32 s77, s75, 0
	v_add_co_u32_e32 v34, vcc, s28, v102
	v_lshl_add_u64 v[104:105], s[46:47], 0, v[178:179]
	s_nop 0
	v_addc_co_u32_e32 v35, vcc, 0, v103, vcc
	v_add_co_u32_e32 v46, vcc, s28, v104
	global_load_dwordx4 v[38:41], v[6:7], off
	global_load_dwordx4 v[22:25], v[6:7], off offset:64
	global_load_dwordx4 v[14:17], v[6:7], off offset:128
	s_nop 0
	global_load_dwordx4 v[6:9], v[6:7], off offset:192
	v_addc_co_u32_e32 v47, vcc, 0, v105, vcc
	v_add_co_u32_e32 v50, vcc, s29, v102
	global_load_dwordx4 v[26:29], v[102:103], off
	s_nop 0
	global_load_dwordx4 v[34:37], v[34:35], off
	v_addc_co_u32_e32 v51, vcc, 0, v103, vcc
	v_add_co_u32_e32 v54, vcc, s30, v102
	global_load_dwordx4 v[42:45], v[104:105], off
	s_nop 0
	global_load_dwordx4 v[46:49], v[46:47], off
	s_waitcnt vmcnt(0)
	v_addc_co_u32_e32 v55, vcc, 0, v103, vcc
	global_load_dwordx4 v[50:53], v[50:51], off
	s_nop 0
	global_load_dwordx4 v[54:57], v[54:55], off
	s_waitcnt vmcnt(5)
	ds_write_b128 v194, v[26:29] offset:33280
	s_waitcnt vmcnt(4)
	ds_write_b128 v194, v[34:37] offset:41984
	s_waitcnt vmcnt(3)
	ds_write_b128 v181, v[42:45]
	s_waitcnt vmcnt(2)
	ds_write_b128 v181, v[46:49] offset:1024
	s_waitcnt vmcnt(0)
	s_waitcnt vmcnt(1)
	ds_write_b128 v194, v[50:53] offset:50688
	s_waitcnt vmcnt(0)
	ds_write_b128 v194, v[54:57] offset:59392
	s_waitcnt lgkmcnt(0)
	s_barrier
	ds_read_b128 v[26:29], v182 offset:33280
	ds_read_b128 v[34:37], v182 offset:33344
	ds_read_b128 v[46:49], v182 offset:37632
	ds_read_b128 v[50:53], v182 offset:37696
	ds_read_b128 v[58:61], v182 offset:41984
	ds_read_b128 v[62:65], v182 offset:42048
	ds_read_b128 v[70:73], v182 offset:46336
	ds_read_b128 v[74:77], v182 offset:46400
	s_waitcnt lgkmcnt(7)
	v_mfma_f32_16x16x32_bf16 v[42:45], v[26:29], v[30:33], 0
	v_mfma_f32_16x16x32_bf16 v[26:29], v[26:29], v[38:41], 0
	s_waitcnt lgkmcnt(5)
	v_mfma_f32_16x16x32_bf16 v[54:57], v[46:49], v[30:33], 0
	v_mfma_f32_16x16x32_bf16 v[46:49], v[46:49], v[38:41], 0
	s_waitcnt lgkmcnt(3)
	v_mfma_f32_16x16x32_bf16 v[66:69], v[58:61], v[30:33], 0
	v_mfma_f32_16x16x32_bf16 v[58:61], v[58:61], v[38:41], 0
	s_waitcnt lgkmcnt(1)
	v_mfma_f32_16x16x32_bf16 v[78:81], v[70:73], v[30:33], 0
	v_mfma_f32_16x16x32_bf16 v[70:73], v[70:73], v[38:41], 0
	v_mfma_f32_16x16x32_bf16 v[42:45], v[34:37], v[18:21], v[42:45]
	v_mfma_f32_16x16x32_bf16 v[26:29], v[34:37], v[22:25], v[26:29]
	v_mfma_f32_16x16x32_bf16 v[34:37], v[50:53], v[18:21], v[54:57]
	v_mfma_f32_16x16x32_bf16 v[46:49], v[50:53], v[22:25], v[46:49]
	v_mfma_f32_16x16x32_bf16 v[50:53], v[62:65], v[18:21], v[66:69]
	v_mfma_f32_16x16x32_bf16 v[54:57], v[62:65], v[22:25], v[58:61]
	s_waitcnt lgkmcnt(0)
	v_mfma_f32_16x16x32_bf16 v[58:61], v[74:77], v[18:21], v[78:81]
	v_mfma_f32_16x16x32_bf16 v[62:65], v[74:77], v[22:25], v[70:73]
	ds_read_b128 v[66:69], v182 offset:33408
	ds_read_b128 v[74:77], v182 offset:33472
	s_waitcnt lgkmcnt(1)
	v_mfma_f32_16x16x32_bf16 v[42:45], v[66:69], v[10:13], v[42:45]
	v_mfma_f32_16x16x32_bf16 v[26:29], v[66:69], v[14:17], v[26:29]
	ds_read_b128 v[66:69], v182 offset:37760
	ds_read_b128 v[78:81], v182 offset:37824
	s_waitcnt lgkmcnt(1)
	v_mfma_f32_16x16x32_bf16 v[34:37], v[66:69], v[10:13], v[34:37]
	v_mfma_f32_16x16x32_bf16 v[46:49], v[66:69], v[14:17], v[46:49]
	ds_read_b128 v[66:69], v182 offset:42112
	ds_read_b128 v[82:85], v182 offset:42176
	s_waitcnt lgkmcnt(1)
	v_mfma_f32_16x16x32_bf16 v[50:53], v[66:69], v[10:13], v[50:53]
	v_mfma_f32_16x16x32_bf16 v[86:89], v[66:69], v[14:17], v[54:57]
	s_nop 2
	ds_read_b128 v[54:57], v182 offset:46464
	ds_read_b128 v[90:93], v182 offset:46528
	v_mfma_f32_16x16x32_bf16 v[66:69], v[74:77], v[6:9], v[26:29]
	s_nop 2
	v_add_co_u32_e32 v26, vcc, s25, v102
	s_waitcnt lgkmcnt(1)
	v_mfma_f32_16x16x32_bf16 v[98:101], v[54:57], v[14:17], v[62:65]
	v_addc_co_u32_e32 v27, vcc, 0, v103, vcc
	v_add_co_u32_e32 v28, vcc, s31, v102
	v_mfma_f32_16x16x32_bf16 v[62:65], v[78:81], v[2:5], v[34:37]
	s_nop 0
	v_addc_co_u32_e32 v29, vcc, 0, v103, vcc
	global_load_dwordx4 v[106:109], v[26:27], off
	global_load_dwordx4 v[110:113], v[28:29], off
	v_add_co_u32_e32 v26, vcc, s29, v104
	v_mfma_f32_16x16x32_bf16 v[94:97], v[54:57], v[10:13], v[58:61]
	s_nop 0
	v_addc_co_u32_e32 v27, vcc, 0, v105, vcc
	v_add_co_u32_e32 v34, vcc, s30, v104
	v_mfma_f32_16x16x32_bf16 v[70:73], v[74:77], v[2:5], v[42:45]
	s_nop 0
	v_addc_co_u32_e32 v35, vcc, 0, v105, vcc
	s_nop 0
	v_mfma_f32_16x16x32_bf16 v[58:61], v[78:81], v[6:9], v[46:49]
	v_mfma_f32_16x16x32_bf16 v[54:57], v[82:85], v[2:5], v[50:53]
	v_mfma_f32_16x16x32_bf16 v[50:53], v[82:85], v[6:9], v[86:89]
	s_waitcnt lgkmcnt(0)
; #define HLOADV(kt) do { const char* vb_ = (const char*)Vh + (size_t)(kt) * (64 * LDK * 2); sv0 = *(const bf16x8*)(vb_ + koff0); sv1 = *(const bf16x8*)(vb_ + koff1); } while (0)
; #define HLOADK(kt) do { const char* kb_ = (const char*)Kh + (size_t)(kt) * (64 * LDK * 2); sk0 = *(const bf16x8*)(kb_ + koff0); sk1 = *(const bf16x8*)(kb_ + koff1); } while (0)
; #define HWRITEV(b) do { char* d_ = V_lds + (b) * G16_V; *(bf16x8*)(d_ + vst0) = sv0; *(bf16x8*)(d_ + vst1) = sv1; } while (0)
; #define HWRITEK(b) do { char* d_ = K_lds + (b) * GB_K; *(bf16x8*)(d_ + KSWZ(sr, sc * 2)) = sk0; *(bf16x8*)(d_ + KSWZ(32 + sr, sc * 2)) = sk1; } while (0)
; #define HEXP() do { _Pragma("unroll") for (int kt = 0; kt < 4; ++kt) { _Pragma("unroll") for (int qt = 0; qt < 2; ++qt) { _Pragma("unroll") for (int i = 0; i < 4; ++i) s[kt][qt][i] = __builtin_amdgcn_exp2f(fmaf(s[kt][qt][i], C, mnC)); } } } while (0)
; template <int LDQ, int LDK, int LDO>
; __device__ __forceinline__ void attn_gqa16_body(const bf16* __restrict__ Qb, const bf16* __restrict__ Kh, const bf16* __restrict__ Vh, bf16* __restrict__ Ob, int seq, char* lds, float mref) {
;     ...
;   float ls0 = 0.f, ls1 = 0.f; f32x4a o[8][2] = {}; bf16x8 qr[2][4];
;   { int l16q = l16, gq = g, widq = wid; asm volatile("" : "+v"(l16q), "+v"(gq), "+v"(widq));
;     const bf16* Qw = Qb + (widq >> 2) * 128 + (long)((widq & 3) * QBLK + l16q) * LDQ + gq * 8;
; #pragma unroll
;     for (int qt = 0; qt < 2; ++qt)
; #pragma unroll
;       for (int ds = 0; ds < 4; ++ds) qr[qt][ds] = *reinterpret_cast<const bf16x8*>(Qw + (long)qt * 16 * LDQ + ds * 32); }
;   const int sr = tid >> 4, sc = (tid & 15) * 8;
;   const int vst0 = (sc >> 4) * VP16 + sr * 32 + ((sc >> 3) & 1) * 16, vst1 = vst0 + 1024;
;   const int vb0 = (int)(uintptr_t)V_lds + (4 * g + (l16 >> 2)) * 32 + (l16 & 3) * 8;
;   const int kb0 = l16 * 272 + g * 16;
;   bf16x8 sv0, sv1, sk0, sk1;
;   const unsigned koff0 = (unsigned)(sr * LDK + sc) * 2u, koff1 = koff0 + 32u * LDK * 2u;
;     ...
;   f32x4a s[4][2]; bf16x8 pb[2][2];
;     ...
;   const int NT = seq / KVBLK;
;   HLOADK(0); HLOADV(0); asm volatile("s_waitcnt vmcnt(0)" ::: "memory"); HWRITEK(0); HWRITEV(0);
;   HLOADK(1); asm volatile("s_waitcnt vmcnt(0)" ::: "memory"); HWRITEK(1); __syncthreads();
;   HLOADK(2); HLOADV(1);
;   HQK(0); HEXP();
;   if (wid >= 4) __builtin_amdgcn_s_setprio(1);
;   for (int t = 0; t < NT; ++t) {
;     HPACK();
	v_mfma_f32_16x16x32_bf16 v[46:49], v[90:93], v[2:5], v[94:97]
	v_mfma_f32_16x16x32_bf16 v[42:45], v[90:93], v[6:9], v[98:101]
	s_and_saveexec_b64 s[16:17], s[4:5]
	s_setprio 1
	s_or_b64 exec, exec, s[16:17]
	v_add_f32_e32 v70, v186, v70
	v_add_f32_e32 v66, v186, v66
	v_add_f32_e32 v62, v186, v62
	v_add_f32_e32 v58, v186, v58
	v_add_f32_e32 v54, v186, v54
	v_add_f32_e32 v50, v186, v50
	v_add_f32_e32 v46, v186, v46
	v_add_f32_e32 v42, v186, v42
	v_exp_f32_e32 v158, v70
	v_add_f32_e32 v70, v186, v71
	v_exp_f32_e32 v159, v66
	v_add_f32_e32 v66, v186, v67
	v_exp_f32_e32 v168, v62
	v_add_f32_e32 v62, v186, v63
	v_exp_f32_e32 v169, v58
	v_add_f32_e32 v58, v186, v59
	v_exp_f32_e32 v142, v54
	v_add_f32_e32 v54, v186, v55
	v_exp_f32_e32 v143, v50
	v_add_f32_e32 v50, v186, v51
	v_exp_f32_e32 v134, v46
	v_add_f32_e32 v46, v186, v47
	v_exp_f32_e32 v135, v42
	v_add_f32_e32 v42, v186, v43
	v_exp_f32_e32 v152, v70
	v_add_f32_e32 v70, v186, v72
	v_exp_f32_e32 v153, v66
	v_add_f32_e32 v66, v186, v68
	v_exp_f32_e32 v170, v62
	v_add_f32_e32 v62, v186, v64
	v_exp_f32_e32 v171, v58
	v_add_f32_e32 v58, v186, v60
	v_exp_f32_e32 v172, v54
	v_add_f32_e32 v54, v186, v56
	v_exp_f32_e32 v173, v50
	v_add_f32_e32 v50, v186, v52
	v_exp_f32_e32 v138, v46
	v_add_f32_e32 v46, v186, v48
	v_exp_f32_e32 v139, v42
	v_add_f32_e32 v42, v186, v44
	v_exp_f32_e32 v156, v70
	v_add_f32_e32 v70, v186, v73
	v_exp_f32_e32 v157, v66
	v_add_f32_e32 v66, v186, v69
	v_exp_f32_e32 v164, v62
	v_add_f32_e32 v62, v186, v65
	v_exp_f32_e32 v165, v58
	v_add_f32_e32 v58, v186, v61
	v_exp_f32_e32 v144, v54
	v_add_f32_e32 v54, v186, v57
	v_exp_f32_e32 v145, v50
	v_add_f32_e32 v50, v186, v53
	v_exp_f32_e32 v136, v46
	v_add_f32_e32 v46, v186, v49
	v_exp_f32_e32 v137, v42
	v_add_f32_e32 v42, v186, v45
	v_exp_f32_e32 v160, v70
	v_exp_f32_e32 v161, v66
	v_exp_f32_e32 v166, v62
	v_exp_f32_e32 v167, v58
	v_exp_f32_e32 v174, v54
	v_exp_f32_e32 v175, v50
	v_exp_f32_e32 v140, v46
	v_exp_f32_e32 v141, v42
	v_mov_b32_e32 v50, 0
	v_lshl_add_u64 v[162:163], s[14:15], 1, v[154:155]
	s_mov_b32 s16, 0
	s_mov_b64 s[14:15], 0
	v_mov_b32_e32 v51, v50
	v_mov_b32_e32 v52, v50
	v_mov_b32_e32 v53, v50
	v_mov_b32_e32 v78, v50
	v_mov_b32_e32 v79, v50
	v_mov_b32_e32 v80, v50
	v_mov_b32_e32 v81, v50
	v_mov_b32_e32 v90, v50
	v_mov_b32_e32 v91, v50
	v_mov_b32_e32 v92, v50
	v_mov_b32_e32 v93, v50
	v_mov_b32_e32 v94, v50
	v_mov_b32_e32 v95, v50
	v_mov_b32_e32 v96, v50
	v_mov_b32_e32 v97, v50
	v_mov_b32_e32 v98, v50
	v_mov_b32_e32 v99, v50
	v_mov_b32_e32 v100, v50
	v_mov_b32_e32 v101, v50
	v_mov_b32_e32 v102, v50
	v_mov_b32_e32 v103, v50
	v_mov_b32_e32 v104, v50
	v_mov_b32_e32 v105, v50
	v_mov_b32_e32 v82, v50
	v_mov_b32_e32 v83, v50
	v_mov_b32_e32 v84, v50
	v_mov_b32_e32 v85, v50
	v_mov_b32_e32 v86, v50
	v_mov_b32_e32 v87, v50
	v_mov_b32_e32 v88, v50
	v_mov_b32_e32 v89, v50
	v_mov_b32_e32 v54, v50
	v_mov_b32_e32 v55, v50
	v_mov_b32_e32 v56, v50
	v_mov_b32_e32 v57, v50
	v_mov_b32_e32 v62, v50
	v_mov_b32_e32 v63, v50
	v_mov_b32_e32 v64, v50
	v_mov_b32_e32 v65, v50
	v_mov_b32_e32 v58, v50
	v_mov_b32_e32 v59, v50
	v_mov_b32_e32 v60, v50
	v_mov_b32_e32 v61, v50
	v_mov_b32_e32 v70, v50
	v_mov_b32_e32 v71, v50
	v_mov_b32_e32 v72, v50
	v_mov_b32_e32 v73, v50
	v_mov_b32_e32 v42, v50
	v_mov_b32_e32 v43, v50
	v_mov_b32_e32 v44, v50
	v_mov_b32_e32 v45, v50
	v_mov_b32_e32 v46, v50
	v_mov_b32_e32 v47, v50
	v_mov_b32_e32 v48, v50
	v_mov_b32_e32 v49, v50
	v_mov_b32_e32 v66, v50
	v_mov_b32_e32 v67, v50
	v_mov_b32_e32 v68, v50
	v_mov_b32_e32 v69, v50
	v_mov_b32_e32 v74, v50
	v_mov_b32_e32 v75, v50
	v_mov_b32_e32 v76, v50
	v_mov_b32_e32 v77, v50
	v_mov_b32_e32 v150, v50
	v_mov_b32_e32 v151, v50
	v_mov_b32_e32 v240, v156
	v_mov_b32_e32 v241, v157
	v_mov_b32_e32 v246, v158
	v_mov_b32_e32 v247, v159
	v_mov_b32_e32 v242, v164
	v_mov_b32_e32 v243, v165
	v_mov_b32_e32 v244, v166
	v_mov_b32_e32 v245, v167
	s_nop 0
	s_nop 0
	s_nop 0
	s_nop 0
	s_nop 0
	s_nop 0
	s_nop 0
.LBB0_650:
	s_add_i32 s17, s16, 1
	s_and_b32 s16, s16, 1
	s_and_b32 s46, 1, s17
	s_cmp_eq_u32 s46, 1
	s_cselect_b32 s85, s86, s84
	s_cselect_b32 s46, 0x4400, 0
	v_add_u32_e32 v189, s46, v182
	v_cvt_pk_bf16_f32 v124, v134, v138
	v_cvt_pk_bf16_f32 v125, v136, v140
	v_cvt_pk_bf16_f32 v128, v135, v139
	v_cvt_pk_bf16_f32 v129, v137, v141
	s_waitcnt vmcnt(2)
	s_barrier
; #define HLOADV(kt) do { const char* vb_ = (const char*)Vh + (size_t)(kt) * (64 * LDK * 2); sv0 = *(const bf16x8*)(vb_ + koff0); sv1 = *(const bf16x8*)(vb_ + koff1); } while (0)
; #define HLOADK(kt) do { const char* kb_ = (const char*)Kh + (size_t)(kt) * (64 * LDK * 2); sk0 = *(const bf16x8*)(kb_ + koff0); sk1 = *(const bf16x8*)(kb_ + koff1); } while (0)
; #define HWRITEV(b) do { char* d_ = V_lds + (b) * G16_V; *(bf16x8*)(d_ + vst0) = sv0; *(bf16x8*)(d_ + vst1) = sv1; } while (0)
; #define HWRITEK(b) do { char* d_ = K_lds + (b) * GB_K; *(bf16x8*)(d_ + KSWZ(sr, sc * 2)) = sk0; *(bf16x8*)(d_ + KSWZ(32 + sr, sc * 2)) = sk1; } while (0)
; #define HEXP() do { _Pragma("unroll") for (int kt = 0; kt < 4; ++kt) { _Pragma("unroll") for (int qt = 0; qt < 2; ++qt) { _Pragma("unroll") for (int i = 0; i < 4; ++i) s[kt][qt][i] = __builtin_amdgcn_exp2f(fmaf(s[kt][qt][i], C, mnC)); } } } while (0)
; template <int LDQ, int LDK, int LDO>
; __device__ __forceinline__ void attn_gqa16_body(const bf16* __restrict__ Qb, const bf16* __restrict__ Kh, const bf16* __restrict__ Vh, bf16* __restrict__ Ob, int seq, char* lds, float mref) {
;     ...
;   const int NT = seq / KVBLK;
;   HLOADK(0); HLOADV(0); asm volatile("s_waitcnt vmcnt(0)" ::: "memory"); HWRITEK(0); HWRITEV(0);
;   HLOADK(1); asm volatile("s_waitcnt vmcnt(0)" ::: "memory"); HWRITEK(1); __syncthreads();
;   HLOADK(2); HLOADV(1);
;   HQK(0); HEXP();
;   if (wid >= 4) __builtin_amdgcn_s_setprio(1);
;   for (int t = 0; t < NT; ++t) {
;     HPACK();
;     __syncthreads();
;     const bool more = t + 1 < NT;
;     if (more) HQK((t + 1) & 1);
	ds_read_b128 v[130:133], v189 offset:33280
	ds_read_b128 v[146:149], v189 offset:33344
	ds_read_b128 v[200:203], v189 offset:37632
	ds_read_b128 v[204:207], v189 offset:37696
	ds_read_b128 v[212:215], v189 offset:41984
	ds_read_b128 v[216:219], v189 offset:42048
	ds_read_b128 v[224:227], v189 offset:46336
	ds_read_b128 v[228:231], v189 offset:46400
	s_mov_b32 m0, s85
	s_nop 0
	global_load_lds_dwordx4 v253, s[74:75]
	s_add_i32 m0, s85, 0x400
	s_nop 0
	global_load_lds_dwordx4 v253, s[76:77]
	s_add_u32 s74, s74, 0x90000
	s_addc_u32 s75, s75, 0
	s_add_u32 s76, s76, 0x90000
	s_addc_u32 s77, s77, 0
	s_waitcnt lgkmcnt(7)
	v_mfma_f32_16x16x32_bf16 v[196:199], v[130:133], v[30:33], v[248:251]
	v_add_f32_e64 v134, v134, v138
	v_add_f32_e64 v135, v135, v139
	v_pk_add_f32 v[136:137], v[136:137], v[140:141]
	s_mul_i32 s46, s16, 0x4100
	v_mfma_f32_16x16x32_bf16 v[130:133], v[130:133], v[38:41], v[248:251]
	v_cvt_pk_bf16_f32 v114, v246, v152
	s_waitcnt lgkmcnt(5)
	v_mfma_f32_16x16x32_bf16 v[208:211], v[200:203], v[30:33], v[248:251]
	v_cvt_pk_bf16_f32 v115, v240, v160
	v_mfma_f32_16x16x32_bf16 v[200:203], v[200:203], v[38:41], v[248:251]
	v_cvt_pk_bf16_f32 v116, v168, v170
	s_waitcnt lgkmcnt(3)
	v_mfma_f32_16x16x32_bf16 v[220:223], v[212:215], v[30:33], v[248:251]
	v_cvt_pk_bf16_f32 v117, v242, v244
	v_mfma_f32_16x16x32_bf16 v[212:215], v[212:215], v[38:41], v[248:251]
	v_cvt_pk_bf16_f32 v118, v247, v153
	s_waitcnt lgkmcnt(1)
	v_mfma_f32_16x16x32_bf16 v[232:235], v[224:227], v[30:33], v[248:251]
	v_cvt_pk_bf16_f32 v119, v241, v161
	v_mfma_f32_16x16x32_bf16 v[224:227], v[224:227], v[38:41], v[248:251]
	v_cvt_pk_bf16_f32 v120, v169, v171
	v_mfma_f32_16x16x32_bf16 v[196:199], v[146:149], v[18:21], v[196:199]
	v_cvt_pk_bf16_f32 v121, v243, v245
	v_mfma_f32_16x16x32_bf16 v[130:133], v[146:149], v[22:25], v[130:133]
	v_cvt_pk_bf16_f32 v122, v142, v172
	v_mfma_f32_16x16x32_bf16 v[146:149], v[204:207], v[18:21], v[208:211]
	v_cvt_pk_bf16_f32 v123, v144, v174
	v_mfma_f32_16x16x32_bf16 v[200:203], v[204:207], v[22:25], v[200:203]
	v_cvt_pk_bf16_f32 v126, v143, v173
	v_mfma_f32_16x16x32_bf16 v[204:207], v[216:219], v[18:21], v[220:223]
	v_cvt_pk_bf16_f32 v127, v145, v175
	v_mfma_f32_16x16x32_bf16 v[208:211], v[216:219], v[22:25], v[212:215]
	s_waitcnt lgkmcnt(0)
	v_mfma_f32_16x16x32_bf16 v[216:219], v[228:231], v[22:25], v[224:227]
	ds_read_b128 v[220:223], v189 offset:33408
	s_nop 1
	ds_read_b128 v[224:227], v189 offset:33472
	v_mfma_f32_16x16x32_bf16 v[212:215], v[228:231], v[18:21], v[232:235]
	s_waitcnt lgkmcnt(1)
	v_mfma_f32_16x16x32_bf16 v[196:199], v[220:223], v[10:13], v[196:199]
	v_mfma_f32_16x16x32_bf16 v[130:133], v[220:223], v[14:17], v[130:133]
	ds_read_b128 v[220:223], v189 offset:37760
	ds_read_b128 v[228:231], v189 offset:37824
	s_waitcnt lgkmcnt(1)
	v_mfma_f32_16x16x32_bf16 v[146:149], v[220:223], v[10:13], v[146:149]
	v_mfma_f32_16x16x32_bf16 v[200:203], v[220:223], v[14:17], v[200:203]
	ds_read_b128 v[220:223], v189 offset:42112
	ds_read_b128 v[232:235], v189 offset:42176
	s_waitcnt lgkmcnt(1)
	v_mfma_f32_16x16x32_bf16 v[204:207], v[220:223], v[10:13], v[204:207]
	v_mfma_f32_16x16x32_bf16 v[208:211], v[220:223], v[14:17], v[208:211]
	ds_read_b128 v[220:223], v189 offset:46464
	ds_read_b128 v[236:239], v189 offset:46528
	v_add_u32_e32 v189, s46, v183
	s_waitcnt lgkmcnt(1)
	v_mfma_f32_16x16x32_bf16 v[212:215], v[220:223], v[10:13], v[212:215]
	v_mfma_f32_16x16x32_bf16 v[216:219], v[220:223], v[14:17], v[216:219]
	v_mfma_f32_16x16x32_bf16 v[220:223], v[224:227], v[6:9], v[130:133]
	s_nop 2
	v_add_f32_e64 v130, v246, v152
	v_add_f32_e64 v131, v247, v153
	v_pk_add_f32 v[132:133], v[240:241], v[160:161]
	v_pk_add_f32 v[152:153], v[168:169], v[170:171]
	v_pk_add_f32 v[156:157], v[242:243], v[244:245]
	v_pk_add_f32 v[158:159], v[142:143], v[172:173]
	v_pk_add_f32 v[160:161], v[144:145], v[174:175]
	v_pk_add_f32 v[130:131], v[130:131], v[132:133]
	v_mfma_f32_16x16x32_bf16 v[142:145], v[232:235], v[2:5], v[204:207]
	v_add_f32_e64 v152, v152, v156
	v_add_f32_e64 v153, v153, v157
	v_pk_add_f32 v[156:157], v[158:159], v[160:161]
	v_pk_add_f32 v[158:159], v[134:135], v[136:137]
	v_mfma_f32_16x16x32_bf16 v[138:141], v[232:235], v[6:9], v[208:211]
	v_add_f32_e64 v150, v150, v130
	v_add_f32_e64 v151, v151, v131
	v_pk_add_f32 v[150:151], v[152:153], v[150:151]
	s_waitcnt lgkmcnt(0)
	v_mfma_f32_16x16x32_bf16 v[134:137], v[236:239], v[2:5], v[212:215]
	v_add_f32_e64 v150, v156, v150
	v_add_f32_e64 v151, v157, v151
	v_pk_add_f32 v[150:151], v[158:159], v[150:151]
	v_mfma_f32_16x16x32_bf16 v[196:199], v[224:227], v[2:5], v[196:199]
	v_mfma_f32_16x16x32_bf16 v[224:227], v[228:231], v[2:5], v[146:149]
	v_mfma_f32_16x16x32_bf16 v[146:149], v[228:231], v[6:9], v[200:203]
	v_mfma_f32_16x16x32_bf16 v[130:133], v[236:239], v[6:9], v[216:219]
	ds_read_b64_tr_b16 v[156:157], v189 offset:0
	ds_read_b64_tr_b16 v[158:159], v189 offset:0x200
	ds_read_b64_tr_b16 v[164:165], v189 offset:0x400
	ds_read_b64_tr_b16 v[166:167], v189 offset:0x600
	ds_read_b64_tr_b16 v[168:169], v189 offset:0x820
	ds_read_b64_tr_b16 v[170:171], v189 offset:0xa20
	ds_read_b64_tr_b16 v[172:173], v189 offset:0xc20
	ds_read_b64_tr_b16 v[174:175], v189 offset:0xe20
	ds_read_b64_tr_b16 v[200:201], v189 offset:0x1040
	ds_read_b64_tr_b16 v[202:203], v189 offset:0x1240
	ds_read_b64_tr_b16 v[204:205], v189 offset:0x1440
	ds_read_b64_tr_b16 v[206:207], v189 offset:0x1640
	s_waitcnt lgkmcnt(4)
; template <int D0> __device__ __forceinline__ void pv16(f32x4a (&o)[8][2], int vb, const bf16x8 (&pb)[2][2]) {
;     ...
;   const s16x4 a0 = TR(D0, 0, 0), a1 = TR(D0, 0, 1), a2 = TR(D0, 1, 0), a3 = TR(D0, 1, 1), b0 = TR(D0 + 1, 0, 0), b1 = TR(D0 + 1, 0, 1), b2 = TR(D0 + 1, 1, 0), b3 = TR(D0 + 1, 1, 1);
;   const s16x4 c0 = TR(D0 + 2, 0, 0), c1 = TR(D0 + 2, 0, 1), c2 = TR(D0 + 2, 1, 0), c3 = TR(D0 + 2, 1, 1);
;   asm volatile("s_waitcnt lgkmcnt(4)" ::: "memory"); SBAR();
;   o[D0][0] = MFMA16(PK16(a0, a1), pb[0][0], o[D0][0]); o[D0][1] = MFMA16(PK16(a0, a1), pb[0][1], o[D0][1]);
;   o[D0 + 1][0] = MFMA16(PK16(b0, b1), pb[0][0], o[D0 + 1][0]); o[D0 + 1][1] = MFMA16(PK16(b0, b1), pb[0][1], o[D0 + 1][1]);
;   o[D0][0] = MFMA16(PK16(a2, a3), pb[1][0], o[D0][0]); o[D0][1] = MFMA16(PK16(a2, a3), pb[1][1], o[D0][1]);
;   o[D0 + 1][0] = MFMA16(PK16(b2, b3), pb[1][0], o[D0 + 1][0]); o[D0 + 1][1] = MFMA16(PK16(b2, b3), pb[1][1], o[D0 + 1][1]);
;   SBAR();
;   const s16x4 d0 = TR(D0 + 3, 0, 0), d1 = TR(D0 + 3, 0, 1), d2 = TR(D0 + 3, 1, 0), d3 = TR(D0 + 3, 1, 1);
;   asm volatile("s_waitcnt lgkmcnt(4)" ::: "memory"); SBAR();
;   o[D0 + 2][0] = MFMA16(PK16(c0, c1), pb[0][0], o[D0 + 2][0]); o[D0 + 2][1] = MFMA16(PK16(c0, c1), pb[0][1], o[D0 + 2][1]);
;   o[D0 + 2][0] = MFMA16(PK16(c2, c3), pb[1][0], o[D0 + 2][0]); o[D0 + 2][1] = MFMA16(PK16(c2, c3), pb[1][1], o[D0 + 2][1]);
;   asm volatile("s_waitcnt lgkmcnt(0)" ::: "memory"); SBAR();
;   o[D0 + 3][0] = MFMA16(PK16(d0, d1), pb[0][0], o[D0 + 3][0]); o[D0 + 3][1] = MFMA16(PK16(d0, d1), pb[0][1], o[D0 + 3][1]);
;   o[D0 + 3][0] = MFMA16(PK16(d2, d3), pb[1][0], o[D0 + 3][0]); o[D0 + 3][1] = MFMA16(PK16(d2, d3), pb[1][1], o[D0 + 3][1]);
; template <int LDQ, int LDK, int LDO>
; __device__ __forceinline__ void attn_gqa16_body(const bf16* __restrict__ Qb, const bf16* __restrict__ Kh, const bf16* __restrict__ Vh, bf16* __restrict__ Ob, int seq, char* lds, float mref) {
;     ...
;     HPACK();
;     __syncthreads();
;     const bool more = t + 1 < NT;
;     if (more) HQK((t + 1) & 1);
;     const int vb = vb0 + (t & 1) * (int)G16_V;
;     SBAR(); pv16<0>(o, vb, pb); SBAR();
;     asm volatile("s_waitcnt vmcnt(0)" ::: "memory");
;     if (t + 2 < NT) HWRITEK(t & 1);
;     if (t + 1 < NT) HWRITEV((t + 1) & 1);
;     HLOADK(t + 3); HLOADV(t + 2);
;     SBAR(); pv16<4>(o, vb, pb); SBAR();
;     if (more) HEXP();
	s_nop 0
	v_mfma_f32_16x16x32_bf16 v[102:105], v[156:159], v[114:117], v[102:105]
	v_mfma_f32_16x16x32_bf16 v[98:101], v[156:159], v[118:121], v[98:101]
	v_mfma_f32_16x16x32_bf16 v[94:97], v[168:171], v[114:117], v[94:97]
	v_exp_f32_e32 v246, v196
	v_mfma_f32_16x16x32_bf16 v[90:93], v[168:171], v[118:121], v[90:93]
	v_exp_f32_e32 v240, v198
	v_mfma_f32_16x16x32_bf16 v[102:105], v[164:167], v[122:125], v[102:105]
	v_exp_f32_e32 v160, v199
	v_mfma_f32_16x16x32_bf16 v[98:101], v[164:167], v[126:129], v[98:101]
	v_exp_f32_e32 v247, v220
	v_mfma_f32_16x16x32_bf16 v[94:97], v[172:175], v[122:125], v[94:97]
	v_exp_f32_e32 v241, v222
	v_mfma_f32_16x16x32_bf16 v[90:93], v[172:175], v[126:129], v[90:93]
	v_exp_f32_e32 v161, v223
	ds_read_b64_tr_b16 v[156:157], v189 offset:0x1860
	ds_read_b64_tr_b16 v[158:159], v189 offset:0x1a60
	ds_read_b64_tr_b16 v[164:165], v189 offset:0x1c60
	ds_read_b64_tr_b16 v[166:167], v189 offset:0x1e60
	s_waitcnt lgkmcnt(4)
	v_mfma_f32_16x16x32_bf16 v[78:81], v[200:203], v[114:117], v[78:81]
	v_exp_f32_e32 v242, v226
	s_waitcnt lgkmcnt(0)
	v_mfma_f32_16x16x32_bf16 v[50:53], v[200:203], v[118:121], v[50:53]
	v_exp_f32_e32 v244, v227
	v_mfma_f32_16x16x32_bf16 v[78:81], v[204:207], v[122:125], v[78:81]
	v_exp_f32_e32 v243, v148
	v_mfma_f32_16x16x32_bf16 v[50:53], v[204:207], v[126:129], v[50:53]
	v_exp_f32_e32 v245, v149
	v_mfma_f32_16x16x32_bf16 v[82:85], v[156:159], v[114:117], v[82:85]
	v_exp_f32_e32 v142, v142
	v_mfma_f32_16x16x32_bf16 v[86:89], v[156:159], v[118:121], v[86:89]
	v_exp_f32_e32 v144, v144
	v_mfma_f32_16x16x32_bf16 v[82:85], v[164:167], v[122:125], v[82:85]
	v_exp_f32_e32 v134, v134
	v_mfma_f32_16x16x32_bf16 v[86:89], v[164:167], v[126:129], v[86:89]
	v_exp_f32_e32 v136, v136
	v_lshl_add_u64 v[152:153], v[162:163], 0, s[14:15]
	v_add_co_u32_e32 v156, vcc, s37, v152
	s_mulk_i32 s16, 0x4400
	s_nop 0
	v_addc_co_u32_e32 v157, vcc, 0, v153, vcc
	v_add_co_u32_e32 v158, vcc, s38, v152
	v_add_u32_e32 v164, s16, v194
	s_nop 0
	v_addc_co_u32_e32 v159, vcc, 0, v153, vcc
	s_waitcnt vmcnt(2)
	ds_write_b128 v164, v[106:109] offset:33280
	ds_write_b128 v164, v[110:113] offset:41984
	global_load_dwordx4 v[106:109], v[156:157], off offset:3072
	global_load_dwordx4 v[110:113], v[158:159], off offset:3072
	ds_read_b64_tr_b16 v[156:157], v189 offset:0x2080
	ds_read_b64_tr_b16 v[158:159], v189 offset:0x2280
	ds_read_b64_tr_b16 v[164:165], v189 offset:0x2480
	ds_read_b64_tr_b16 v[166:167], v189 offset:0x2680
	ds_read_b64_tr_b16 v[168:169], v189 offset:0x28a0
	ds_read_b64_tr_b16 v[170:171], v189 offset:0x2aa0
	ds_read_b64_tr_b16 v[172:173], v189 offset:0x2ca0
	ds_read_b64_tr_b16 v[174:175], v189 offset:0x2ea0
	ds_read_b64_tr_b16 v[200:201], v189 offset:0x30c0
	ds_read_b64_tr_b16 v[202:203], v189 offset:0x32c0
	ds_read_b64_tr_b16 v[204:205], v189 offset:0x34c0
	ds_read_b64_tr_b16 v[206:207], v189 offset:0x36c0
	s_waitcnt lgkmcnt(4)
	s_nop 0
	v_mfma_f32_16x16x32_bf16 v[54:57], v[156:159], v[114:117], v[54:57]
	v_exp_f32_e32 v152, v197
	v_mfma_f32_16x16x32_bf16 v[62:65], v[156:159], v[118:121], v[62:65]
	v_exp_f32_e32 v153, v221
	v_mfma_f32_16x16x32_bf16 v[58:61], v[168:171], v[114:117], v[58:61]
	v_mfma_f32_16x16x32_bf16 v[70:73], v[168:171], v[118:121], v[70:73]
	v_mfma_f32_16x16x32_bf16 v[54:57], v[164:167], v[122:125], v[54:57]
	v_mfma_f32_16x16x32_bf16 v[62:65], v[164:167], v[126:129], v[62:65]
	v_mfma_f32_16x16x32_bf16 v[58:61], v[172:175], v[122:125], v[58:61]
	v_mfma_f32_16x16x32_bf16 v[70:73], v[172:175], v[126:129], v[70:73]
	ds_read_b64_tr_b16 v[156:157], v189 offset:0x38e0
	ds_read_b64_tr_b16 v[158:159], v189 offset:0x3ae0
	ds_read_b64_tr_b16 v[164:165], v189 offset:0x3ce0
	ds_read_b64_tr_b16 v[166:167], v189 offset:0x3ee0
	s_waitcnt lgkmcnt(4)
	v_mfma_f32_16x16x32_bf16 v[42:45], v[200:203], v[114:117], v[42:45]
	v_exp_f32_e32 v168, v224
	v_exp_f32_e32 v170, v225
	s_waitcnt lgkmcnt(0)
	v_mfma_f32_16x16x32_bf16 v[46:49], v[200:203], v[118:121], v[46:49]
	v_exp_f32_e32 v169, v146
	v_exp_f32_e32 v171, v147
	v_mfma_f32_16x16x32_bf16 v[42:45], v[204:207], v[122:125], v[42:45]
	v_exp_f32_e32 v172, v143
	v_exp_f32_e32 v174, v145
	v_mfma_f32_16x16x32_bf16 v[46:49], v[204:207], v[126:129], v[46:49]
	v_exp_f32_e32 v143, v138
	v_exp_f32_e32 v173, v139
	v_mfma_f32_16x16x32_bf16 v[66:69], v[156:159], v[114:117], v[66:69]
	v_exp_f32_e32 v145, v140
	v_exp_f32_e32 v175, v141
	v_mfma_f32_16x16x32_bf16 v[74:77], v[156:159], v[118:121], v[74:77]
	v_exp_f32_e32 v138, v135
	v_exp_f32_e32 v140, v137
	v_mfma_f32_16x16x32_bf16 v[66:69], v[164:167], v[122:125], v[66:69]
	v_exp_f32_e32 v135, v130
	v_exp_f32_e32 v139, v131
	v_mfma_f32_16x16x32_bf16 v[74:77], v[164:167], v[126:129], v[74:77]
	v_exp_f32_e32 v137, v132
	v_exp_f32_e32 v141, v133
	s_add_u32 s14, s14, 0x90000
	s_addc_u32 s15, s15, 0
	s_cmp_lg_u32 s14, 0x9120000
	s_mov_b32 s16, s17
	s_cbranch_scc1 .LBB0_650
	v_mov_b32_e32 v156, v240
	v_mov_b32_e32 v157, v241
	v_mov_b32_e32 v158, v246
	v_mov_b32_e32 v159, v247
	v_mov_b32_e32 v164, v242
	v_mov_b32_e32 v165, v243
	v_mov_b32_e32 v166, v244
	v_mov_b32_e32 v167, v245
	s_waitcnt vmcnt(1)
	v_cvt_pk_bf16_f32 v106, v158, v152
	v_cvt_pk_bf16_f32 v107, v156, v160
	v_cvt_pk_bf16_f32 v108, v168, v170
	v_cvt_pk_bf16_f32 v109, v164, v166
	s_waitcnt vmcnt(0)
	v_cvt_pk_bf16_f32 v110, v159, v153
	v_cvt_pk_bf16_f32 v111, v157, v161
	v_cvt_pk_bf16_f32 v112, v169, v171
	v_cvt_pk_bf16_f32 v113, v165, v167
	v_cvt_pk_bf16_f32 v114, v142, v172
	v_cvt_pk_bf16_f32 v115, v144, v174
	v_cvt_pk_bf16_f32 v116, v134, v138
	v_cvt_pk_bf16_f32 v117, v136, v140
	v_cvt_pk_bf16_f32 v118, v143, v173
	v_cvt_pk_bf16_f32 v119, v145, v175
	v_cvt_pk_bf16_f32 v120, v135, v139
	v_cvt_pk_bf16_f32 v121, v137, v141
	s_waitcnt lgkmcnt(0)
	s_barrier
; #define SBAR() __builtin_amdgcn_sched_barrier(0)
; #define HLOADV(kt) do { const char* vb_ = (const char*)Vh + (size_t)(kt) * (64 * LDK * 2); sv0 = *(const bf16x8*)(vb_ + koff0); sv1 = *(const bf16x8*)(vb_ + koff1); } while (0)
; #define HLOADK(kt) do { const char* kb_ = (const char*)Kh + (size_t)(kt) * (64 * LDK * 2); sk0 = *(const bf16x8*)(kb_ + koff0); sk1 = *(const bf16x8*)(kb_ + koff1); } while (0)
; #define HWRITEV(b) do { char* d_ = V_lds + (b) * G16_V; *(bf16x8*)(d_ + vst0) = sv0; *(bf16x8*)(d_ + vst1) = sv1; } while (0)
; #define HWRITEK(b) do { char* d_ = K_lds + (b) * GB_K; *(bf16x8*)(d_ + KSWZ(sr, sc * 2)) = sk0; *(bf16x8*)(d_ + KSWZ(32 + sr, sc * 2)) = sk1; } while (0)
; template <int LDQ, int LDK, int LDO>
; __device__ __forceinline__ void attn_gqa16_body(const bf16* __restrict__ Qb, const bf16* __restrict__ Kh, const bf16* __restrict__ Vh, bf16* __restrict__ Ob, int seq, char* lds, float mref) {
;     ...
;     HPACK();
;     __syncthreads();
;     const bool more = t + 1 < NT;
;     if (more) HQK((t + 1) & 1);
;     const int vb = vb0 + (t & 1) * (int)G16_V;
;     SBAR(); pv16<0>(o, vb, pb); SBAR();
;     asm volatile("s_waitcnt vmcnt(0)" ::: "memory");
;     if (t + 2 < NT) HWRITEK(t & 1);
;     if (t + 1 < NT) HWRITEV((t + 1) & 1);
;     HLOADK(t + 3); HLOADV(t + 2);
;     SBAR(); pv16<4>(o, vb, pb); SBAR();
	s_mov_b32 m0, s86
	s_nop 0
	global_load_lds_dwordx4 v253, s[74:75]
	s_add_i32 m0, s86, 0x400
	s_nop 0
	global_load_lds_dwordx4 v253, s[76:77]
	ds_read_b128 v[122:125], v182 offset:50688
	ds_read_b128 v[126:129], v182 offset:50752
	ds_read_b128 v[146:149], v182 offset:55040
	ds_read_b128 v[196:199], v182 offset:55104
	ds_read_b128 v[204:207], v182 offset:59392
	ds_read_b128 v[208:211], v182 offset:59456
	ds_read_b128 v[216:219], v182 offset:63744
	ds_read_b128 v[220:223], v182 offset:63808
	s_waitcnt lgkmcnt(7)
	v_mfma_f32_16x16x32_bf16 v[130:133], v[122:125], v[30:33], 0
	v_mov_b32_e32 v190, v168
	v_mov_b32_e32 v191, v158
	v_mov_b32_e32 v192, v170
	v_mfma_f32_16x16x32_bf16 v[122:125], v[122:125], v[38:41], 0
	v_mov_b32_e32 v193, v152
	v_mov_b32_e32 v152, v171
	s_lshl_b32 s8, s8, 12
	s_waitcnt lgkmcnt(5)
	v_mfma_f32_16x16x32_bf16 v[200:203], v[146:149], v[30:33], 0
	s_add_u32 s8, s42, s8
	s_addc_u32 s14, s43, 0
	s_add_u32 s12, s8, s12
	v_mfma_f32_16x16x32_bf16 v[146:149], v[146:149], v[38:41], 0
	s_addc_u32 s13, s14, s13
	s_waitcnt lgkmcnt(3)
	v_mfma_f32_16x16x32_bf16 v[212:215], v[204:207], v[30:33], 0
	s_waitcnt lgkmcnt(1)
	v_mfma_f32_16x16x32_bf16 v[30:33], v[216:219], v[30:33], 0
	v_mfma_f32_16x16x32_bf16 v[130:133], v[126:129], v[18:21], v[130:133]
	v_mfma_f32_16x16x32_bf16 v[122:125], v[126:129], v[22:25], v[122:125]
	v_mfma_f32_16x16x32_bf16 v[126:129], v[196:199], v[18:21], v[200:203]
	v_mfma_f32_16x16x32_bf16 v[146:149], v[196:199], v[22:25], v[146:149]
	v_mfma_f32_16x16x32_bf16 v[196:199], v[208:211], v[18:21], v[212:215]
	s_waitcnt lgkmcnt(0)
	v_mfma_f32_16x16x32_bf16 v[18:21], v[220:223], v[18:21], v[30:33]
	s_nop 0
	v_mov_b32_e32 v213, v156
	v_mov_b32_e32 v212, v164
	v_mov_b32_e32 v214, v166
	ds_read_b128 v[30:33], v182 offset:50816
	v_mfma_f32_16x16x32_bf16 v[204:207], v[204:207], v[38:41], 0
	v_mov_b32_e32 v215, v160
	v_mfma_f32_16x16x32_bf16 v[38:41], v[216:219], v[38:41], 0
	v_mov_b32_e32 v216, v169
	v_mov_b32_e32 v217, v159
	v_mov_b32_e32 v219, v157
	v_mfma_f32_16x16x32_bf16 v[200:203], v[208:211], v[22:25], v[204:207]
	v_mov_b32_e32 v218, v165
	v_mfma_f32_16x16x32_bf16 v[22:25], v[220:223], v[22:25], v[38:41]
	s_nop 2
	ds_read_b128 v[38:41], v182 offset:55168
	ds_read_b128 v[204:207], v182 offset:50880
	s_waitcnt lgkmcnt(2)
	v_mfma_f32_16x16x32_bf16 v[130:133], v[30:33], v[10:13], v[130:133]
	v_mfma_f32_16x16x32_bf16 v[30:33], v[30:33], v[14:17], v[122:125]
	s_nop 2
	ds_read_b128 v[122:125], v182 offset:59520
	ds_read_b128 v[208:211], v182 offset:55232
	s_waitcnt lgkmcnt(3)
	v_mfma_f32_16x16x32_bf16 v[126:129], v[38:41], v[10:13], v[126:129]
	v_mfma_f32_16x16x32_bf16 v[38:41], v[38:41], v[14:17], v[146:149]
	s_nop 2
	ds_read_b128 v[146:149], v182 offset:63872
	ds_read_b128 v[168:171], v182 offset:59584
	ds_read_b128 v[156:159], v182 offset:63936
	s_waitcnt lgkmcnt(4)
	v_mfma_f32_16x16x32_bf16 v[196:199], v[122:125], v[10:13], v[196:199]
	s_waitcnt lgkmcnt(2)
	v_mfma_f32_16x16x32_bf16 v[10:13], v[146:149], v[10:13], v[18:21]
	v_mfma_f32_16x16x32_bf16 v[122:125], v[122:125], v[14:17], v[200:203]
	s_nop 1
	v_mov_b32_e32 v18, v142
	v_mov_b32_e32 v19, v144
	v_mov_b32_e32 v20, v172
	v_mfma_f32_16x16x32_bf16 v[14:17], v[146:149], v[14:17], v[22:25]
	v_mov_b32_e32 v201, v161
	v_mov_b32_e32 v200, v167
	v_mov_b32_e32 v21, v174
	v_mfma_f32_16x16x32_bf16 v[160:163], v[204:207], v[6:9], v[30:33]
	v_add_f32_e64 v24, v190, v192
	v_add_f32_e64 v25, v191, v193
	v_mov_b32_e32 v144, v143
	v_mov_b32_e32 v22, v173
	v_pk_add_f32 v[30:31], v[212:213], v[214:215]
	v_mfma_f32_16x16x32_bf16 v[146:149], v[204:207], v[2:5], v[130:133]
	v_add_f32_e64 v24, v24, v30
	v_add_f32_e64 v25, v25, v31
	v_mov_b32_e32 v23, v175
	v_pk_add_f32 v[32:33], v[216:217], v[152:153]
	v_mfma_f32_16x16x32_bf16 v[164:167], v[208:211], v[2:5], v[126:129]
	v_add_f32_e64 v144, v144, v22
	v_add_f32_e64 v145, v145, v23
	v_add_f32_e32 v130, v134, v138
	v_add_f32_e32 v132, v136, v140
	v_mfma_f32_16x16x32_bf16 v[172:175], v[208:211], v[6:9], v[38:41]
	v_add_f32_e64 v126, v18, v20
	v_add_f32_e64 v127, v19, v21
	s_nop 0
	v_pk_add_f32 v[38:39], v[218:219], v[200:201]
	s_waitcnt lgkmcnt(1)
	v_mfma_f32_16x16x32_bf16 v[196:199], v[168:171], v[2:5], v[196:199]
	v_add_f32_e64 v142, v32, v38
	v_add_f32_e64 v143, v33, v39
	s_waitcnt lgkmcnt(0)
	v_mfma_f32_16x16x32_bf16 v[200:203], v[156:159], v[2:5], v[10:13]
	v_add_f32_e64 v2, v150, v25
	v_add_f32_e64 v3, v151, v24
	v_pk_add_f32 v[128:129], v[24:25], v[2:3]
	v_mfma_f32_16x16x32_bf16 v[168:171], v[168:171], v[6:9], v[122:125]
	s_nop 2
	v_add_f32_e32 v122, v135, v139
	v_add_f32_e32 v124, v137, v141
	v_mfma_f32_16x16x32_bf16 v[134:137], v[156:159], v[6:9], v[14:17]
	ds_read_b64_tr_b16 v[2:3], v183 offset:0
	ds_read_b64_tr_b16 v[4:5], v183 offset:0x200
	ds_read_b64_tr_b16 v[6:7], v183 offset:0x400
	ds_read_b64_tr_b16 v[8:9], v183 offset:0x600
	ds_read_b64_tr_b16 v[10:11], v183 offset:0x820
	ds_read_b64_tr_b16 v[12:13], v183 offset:0xa20
	ds_read_b64_tr_b16 v[14:15], v183 offset:0xc20
	ds_read_b64_tr_b16 v[16:17], v183 offset:0xe20
	ds_read_b64_tr_b16 v[18:19], v183 offset:0x1040
	ds_read_b64_tr_b16 v[20:21], v183 offset:0x1240
	ds_read_b64_tr_b16 v[22:23], v183 offset:0x1440
	ds_read_b64_tr_b16 v[24:25], v183 offset:0x1640
	s_waitcnt lgkmcnt(4)
	s_nop 0
	v_mfma_f32_16x16x32_bf16 v[30:33], v[2:5], v[106:109], v[102:105]
	v_mfma_f32_16x16x32_bf16 v[38:41], v[2:5], v[110:113], v[98:101]
	v_mfma_f32_16x16x32_bf16 v[94:97], v[10:13], v[106:109], v[94:97]
	v_mfma_f32_16x16x32_bf16 v[10:13], v[10:13], v[110:113], v[90:93]
	v_mfma_f32_16x16x32_bf16 v[2:5], v[6:9], v[114:117], v[30:33]
	v_mfma_f32_16x16x32_bf16 v[6:9], v[6:9], v[118:121], v[38:41]
	v_mfma_f32_16x16x32_bf16 v[38:41], v[14:17], v[114:117], v[94:97]
	v_mfma_f32_16x16x32_bf16 v[90:93], v[14:17], v[118:121], v[10:13]
	ds_read_b64_tr_b16 v[14:15], v183 offset:0x1860
	ds_read_b64_tr_b16 v[16:17], v183 offset:0x1a60
	ds_read_b64_tr_b16 v[30:31], v183 offset:0x1c60
	ds_read_b64_tr_b16 v[32:33], v183 offset:0x1e60
	s_waitcnt lgkmcnt(4)
; #define SBAR() __builtin_amdgcn_sched_barrier(0)
; #define HLOADV(kt) do { const char* vb_ = (const char*)Vh + (size_t)(kt) * (64 * LDK * 2); sv0 = *(const bf16x8*)(vb_ + koff0); sv1 = *(const bf16x8*)(vb_ + koff1); } while (0)
; #define HLOADK(kt) do { const char* kb_ = (const char*)Kh + (size_t)(kt) * (64 * LDK * 2); sk0 = *(const bf16x8*)(kb_ + koff0); sk1 = *(const bf16x8*)(kb_ + koff1); } while (0)
; #define HWRITEV(b) do { char* d_ = V_lds + (b) * G16_V; *(bf16x8*)(d_ + vst0) = sv0; *(bf16x8*)(d_ + vst1) = sv1; } while (0)
; #define HWRITEK(b) do { char* d_ = K_lds + (b) * GB_K; *(bf16x8*)(d_ + KSWZ(sr, sc * 2)) = sk0; *(bf16x8*)(d_ + KSWZ(32 + sr, sc * 2)) = sk1; } while (0)
; #define HEXP() do { _Pragma("unroll") for (int kt = 0; kt < 4; ++kt) { _Pragma("unroll") for (int qt = 0; qt < 2; ++qt) { _Pragma("unroll") for (int i = 0; i < 4; ++i) s[kt][qt][i] = __builtin_amdgcn_exp2f(fmaf(s[kt][qt][i], C, mnC)); } } } while (0)
; template <int LDQ, int LDK, int LDO>
; __device__ __forceinline__ void attn_gqa16_body(const bf16* __restrict__ Qb, const bf16* __restrict__ Kh, const bf16* __restrict__ Vh, bf16* __restrict__ Ob, int seq, char* lds, float mref) {
;     ...
;     SBAR(); pv16<0>(o, vb, pb); SBAR();
;     asm volatile("s_waitcnt vmcnt(0)" ::: "memory");
;     if (t + 2 < NT) HWRITEK(t & 1);
;     if (t + 1 < NT) HWRITEV((t + 1) & 1);
;     HLOADK(t + 3); HLOADV(t + 2);
;     SBAR(); pv16<4>(o, vb, pb); SBAR();
;     if (more) HEXP();
	v_mfma_f32_16x16x32_bf16 v[10:13], v[18:21], v[106:109], v[78:81]
	s_waitcnt lgkmcnt(0)
	v_mfma_f32_16x16x32_bf16 v[18:21], v[18:21], v[110:113], v[50:53]
	v_mfma_f32_16x16x32_bf16 v[10:13], v[22:25], v[114:117], v[10:13]
	v_mfma_f32_16x16x32_bf16 v[22:25], v[22:25], v[118:121], v[18:21]
	v_mfma_f32_16x16x32_bf16 v[18:21], v[14:17], v[106:109], v[82:85]
	v_mfma_f32_16x16x32_bf16 v[50:53], v[14:17], v[110:113], v[86:89]
	v_mfma_f32_16x16x32_bf16 v[14:17], v[30:33], v[114:117], v[18:21]
	v_mfma_f32_16x16x32_bf16 v[18:21], v[30:33], v[118:121], v[50:53]
	s_waitcnt vmcnt(0)
	s_waitcnt vmcnt(1)
	s_waitcnt vmcnt(0)
	ds_read_b64_tr_b16 v[26:27], v183 offset:0x2080
	ds_read_b64_tr_b16 v[28:29], v183 offset:0x2280
	ds_read_b64_tr_b16 v[30:31], v183 offset:0x2480
	ds_read_b64_tr_b16 v[32:33], v183 offset:0x2680
	ds_read_b64_tr_b16 v[34:35], v183 offset:0x28a0
	ds_read_b64_tr_b16 v[36:37], v183 offset:0x2aa0
	ds_read_b64_tr_b16 v[78:79], v183 offset:0x2ca0
	ds_read_b64_tr_b16 v[80:81], v183 offset:0x2ea0
	ds_read_b64_tr_b16 v[82:83], v183 offset:0x30c0
	ds_read_b64_tr_b16 v[84:85], v183 offset:0x32c0
	ds_read_b64_tr_b16 v[86:87], v183 offset:0x34c0
	ds_read_b64_tr_b16 v[88:89], v183 offset:0x36c0
	s_waitcnt lgkmcnt(4)
	s_nop 0
	v_mfma_f32_16x16x32_bf16 v[50:53], v[26:29], v[106:109], v[54:57]
	v_mfma_f32_16x16x32_bf16 v[26:29], v[26:29], v[110:113], v[62:65]
	v_mfma_f32_16x16x32_bf16 v[58:61], v[34:37], v[106:109], v[58:61]
	v_mfma_f32_16x16x32_bf16 v[34:37], v[34:37], v[110:113], v[70:73]
	v_mfma_f32_16x16x32_bf16 v[50:53], v[30:33], v[114:117], v[50:53]
	v_mfma_f32_16x16x32_bf16 v[54:57], v[30:33], v[118:121], v[26:29]
	v_mfma_f32_16x16x32_bf16 v[70:73], v[78:81], v[114:117], v[58:61]
	v_mfma_f32_16x16x32_bf16 v[78:81], v[78:81], v[118:121], v[34:37]
	ds_read_b64_tr_b16 v[30:31], v183 offset:0x38e0
	ds_read_b64_tr_b16 v[32:33], v183 offset:0x3ae0
	ds_read_b64_tr_b16 v[34:35], v183 offset:0x3ce0
	ds_read_b64_tr_b16 v[36:37], v183 offset:0x3ee0
	s_waitcnt lgkmcnt(4)
	v_mfma_f32_16x16x32_bf16 v[26:29], v[82:85], v[106:109], v[42:45]
	s_waitcnt lgkmcnt(0)
	v_mfma_f32_16x16x32_bf16 v[42:45], v[82:85], v[110:113], v[46:49]
	v_mfma_f32_16x16x32_bf16 v[26:29], v[86:89], v[114:117], v[26:29]
	v_mfma_f32_16x16x32_bf16 v[58:61], v[86:89], v[118:121], v[42:45]
	v_mfma_f32_16x16x32_bf16 v[42:45], v[30:33], v[106:109], v[66:69]
	v_mfma_f32_16x16x32_bf16 v[46:49], v[30:33], v[110:113], v[74:77]
	v_mfma_f32_16x16x32_bf16 v[30:33], v[34:37], v[114:117], v[42:45]
	v_mfma_f32_16x16x32_bf16 v[62:65], v[34:37], v[118:121], v[46:49]
	s_nop 4
	v_add_f32_e32 v42, v186, v196
	v_exp_f32_e32 v116, v42
	v_add_f32_e32 v42, v186, v197
	v_exp_f32_e32 v117, v42
	v_add_f32_e32 v42, v186, v198
	v_exp_f32_e32 v118, v42
	v_add_f32_e32 v42, v186, v199
	v_exp_f32_e32 v119, v42
	v_add_f32_e32 v42, v186, v168
	v_add_f32_e32 v34, v186, v146
	v_exp_f32_e32 v98, v42
	v_add_f32_e32 v42, v186, v169
	v_exp_f32_e32 v131, v34
	v_add_f32_e32 v34, v186, v147
	v_exp_f32_e32 v99, v42
	v_add_f32_e32 v42, v186, v170
	v_exp_f32_e32 v133, v34
	v_add_f32_e32 v34, v186, v148
	v_exp_f32_e32 v100, v42
	v_add_f32_e32 v42, v186, v171
	v_exp_f32_e32 v74, v34
	v_add_f32_e32 v34, v186, v149
	v_exp_f32_e32 v101, v42
	v_add_f32_e32 v42, v186, v200
	v_exp_f32_e32 v129, v34
	v_add_f32_e32 v34, v186, v160
	v_exp_f32_e32 v120, v42
	v_add_f32_e32 v42, v186, v201
	v_exp_f32_e32 v123, v34
	v_add_f32_e32 v34, v186, v161
	v_exp_f32_e32 v121, v42
	v_add_f32_e32 v42, v186, v202
	v_exp_f32_e32 v125, v34
	v_add_f32_e32 v34, v186, v162
	v_exp_f32_e32 v75, v42
	v_add_f32_e32 v42, v186, v203
	v_exp_f32_e32 v76, v34
	v_add_f32_e32 v34, v186, v163
	v_exp_f32_e32 v77, v42
	v_add_f32_e32 v42, v186, v134
	v_exp_f32_e32 v87, v34
	v_add_f32_e32 v34, v186, v164
	v_exp_f32_e32 v102, v42
	v_add_f32_e32 v42, v186, v135
	v_exp_f32_e32 v66, v34
	v_add_f32_e32 v34, v186, v165
	v_exp_f32_e32 v103, v42
	v_add_f32_e32 v42, v186, v136
	v_exp_f32_e32 v68, v34
	v_add_f32_e32 v34, v186, v166
	v_exp_f32_e32 v43, v42
	v_exp_f32_e32 v67, v34
	v_add_f32_e32 v34, v186, v167
	v_add_f32_e32 v35, v186, v173
	v_exp_f32_e32 v69, v34
	v_add_f32_e32 v34, v186, v172
	v_exp_f32_e32 v36, v35
	v_add_f32_e32 v35, v186, v174
	v_add_f32_e32 v37, v186, v175
	v_add_f32_e32 v42, v186, v137
	v_exp_f32_e32 v34, v34
	v_exp_f32_e32 v35, v35
	v_exp_f32_e32 v37, v37
	v_exp_f32_e32 v45, v42
	v_add_f32_e32 v42, v143, v151
	v_pk_add_f32 v[48:49], v[144:145], v[144:145] op_sel:[0,1] op_sel_hi:[1,0]
	v_pk_add_f32 v[84:85], v[142:143], v[42:43] op_sel_hi:[1,0]
	v_mov_b32_e32 v49, v76
	v_mov_b32_e32 v85, v87
	v_pk_add_f32 v[46:47], v[122:123], v[124:125]
	v_pk_add_f32 v[48:49], v[48:49], v[84:85]
	v_add_f32_e32 v42, v98, v99
	v_pk_add_f32 v[46:47], v[46:47], v[48:49]
	v_pk_add_f32 v[48:49], v[34:35], v[36:37]
	v_pk_add_f32 v[46:47], v[46:47], v[46:47] op_sel:[0,1] op_sel_hi:[1,0]
	v_pk_add_f32 v[48:49], v[48:49], v[48:49] op_sel:[0,1] op_sel_hi:[1,0]
	v_add_f32_e32 v44, v100, v101
	v_mov_b32_e32 v47, v102
	v_mov_b32_e32 v49, v103
	v_pk_add_f32 v[46:47], v[46:47], v[48:49]
	v_pk_add_f32 v[48:49], v[42:43], v[44:45]
	v_cvt_pk_bf16_f32 v82, v131, v133
	v_cvt_pk_bf16_f32 v83, v74, v129
	v_cvt_pk_bf16_f32 v84, v66, v68
	v_cvt_pk_bf16_f32 v85, v67, v69
	v_cvt_pk_bf16_f32 v86, v123, v125
	s_nop 0
	v_pk_add_f32 v[46:47], v[46:47], v[48:49]
	v_pk_add_f32 v[48:49], v[126:127], v[126:127] op_sel:[0,1] op_sel_hi:[1,0]
	v_add_f32_e32 v122, v46, v47
	v_mov_b32_e32 v49, v74
	v_pk_add_f32 v[46:47], v[130:131], v[132:133]
	v_pk_add_f32 v[48:49], v[48:49], v[128:129]
	v_cvt_pk_bf16_f32 v87, v76, v87
	v_cvt_pk_bf16_f32 v88, v34, v36
	v_cvt_pk_bf16_f32 v89, v35, v37
	v_cvt_pk_bf16_f32 v94, v116, v117
	v_cvt_pk_bf16_f32 v95, v118, v119
	s_nop 0
	v_pk_add_f32 v[114:115], v[46:47], v[48:49]
	v_cvt_pk_bf16_f32 v96, v120, v121
	v_cvt_pk_bf16_f32 v97, v75, v77
	v_cvt_pk_bf16_f32 v98, v98, v99
	v_cvt_pk_bf16_f32 v99, v100, v101
	v_cvt_pk_bf16_f32 v100, v102, v103
	v_cvt_pk_bf16_f32 v101, v43, v45
	s_waitcnt lgkmcnt(0)
	s_barrier
; #define SBAR() __builtin_amdgcn_sched_barrier(0)
; #define MFMA16(a, b, c) __builtin_amdgcn_mfma_f32_16x16x32_bf16(a, b, c, 0, 0, 0)
; template <int D0> __device__ __forceinline__ void pv16(f32x4a (&o)[8][2], int vb, const bf16x8 (&pb)[2][2]) {
;     ...
;   const s16x4 a0 = TR(D0, 0, 0), a1 = TR(D0, 0, 1), a2 = TR(D0, 1, 0), a3 = TR(D0, 1, 1), b0 = TR(D0 + 1, 0, 0), b1 = TR(D0 + 1, 0, 1), b2 = TR(D0 + 1, 1, 0), b3 = TR(D0 + 1, 1, 1);
;   const s16x4 c0 = TR(D0 + 2, 0, 0), c1 = TR(D0 + 2, 0, 1), c2 = TR(D0 + 2, 1, 0), c3 = TR(D0 + 2, 1, 1);
;   asm volatile("s_waitcnt lgkmcnt(4)" ::: "memory"); SBAR();
;   o[D0][0] = MFMA16(PK16(a0, a1), pb[0][0], o[D0][0]); o[D0][1] = MFMA16(PK16(a0, a1), pb[0][1], o[D0][1]);
;   o[D0 + 1][0] = MFMA16(PK16(b0, b1), pb[0][0], o[D0 + 1][0]); o[D0 + 1][1] = MFMA16(PK16(b0, b1), pb[0][1], o[D0 + 1][1]);
;   o[D0][0] = MFMA16(PK16(a2, a3), pb[1][0], o[D0][0]); o[D0][1] = MFMA16(PK16(a2, a3), pb[1][1], o[D0][1]);
;   o[D0 + 1][0] = MFMA16(PK16(b2, b3), pb[1][0], o[D0 + 1][0]); o[D0 + 1][1] = MFMA16(PK16(b2, b3), pb[1][1], o[D0 + 1][1]);
;   SBAR();
;   const s16x4 d0 = TR(D0 + 3, 0, 0), d1 = TR(D0 + 3, 0, 1), d2 = TR(D0 + 3, 1, 0), d3 = TR(D0 + 3, 1, 1);
;   asm volatile("s_waitcnt lgkmcnt(4)" ::: "memory"); SBAR();
;   o[D0 + 2][0] = MFMA16(PK16(c0, c1), pb[0][0], o[D0 + 2][0]); o[D0 + 2][1] = MFMA16(PK16(c0, c1), pb[0][1], o[D0 + 2][1]);
;   o[D0 + 2][0] = MFMA16(PK16(c2, c3), pb[1][0], o[D0 + 2][0]); o[D0 + 2][1] = MFMA16(PK16(c2, c3), pb[1][1], o[D0 + 2][1]);
;   asm volatile("s_waitcnt lgkmcnt(0)" ::: "memory"); SBAR();
;   o[D0 + 3][0] = MFMA16(PK16(d0, d1), pb[0][0], o[D0 + 3][0]); o[D0 + 3][1] = MFMA16(PK16(d0, d1), pb[0][1], o[D0 + 3][1]);
;   o[D0 + 3][0] = MFMA16(PK16(d2, d3), pb[1][0], o[D0 + 3][0]); o[D0 + 3][1] = MFMA16(PK16(d2, d3), pb[1][1], o[D0 + 3][1]);
; template <int LDQ, int LDK, int LDO>
; __device__ __forceinline__ void attn_gqa16_body(const bf16* __restrict__ Qb, const bf16* __restrict__ Kh, const bf16* __restrict__ Vh, bf16* __restrict__ Ob, int seq, char* lds, float mref) {
;     ...
;     SBAR(); pv16<4>(o, vb, pb); SBAR();
;     if (more) HEXP();
;   }
;   __builtin_amdgcn_s_setprio(0);
;   ls0 += __shfl_xor(ls0, 16); ls0 += __shfl_xor(ls0, 32); ls1 += __shfl_xor(ls1, 16); ls1 += __shfl_xor(ls1, 32);
;   const float rl[2] = {__builtin_amdgcn_rcpf(ls0), __builtin_amdgcn_rcpf(ls1)};
	ds_read_b64_tr_b16 v[34:35], v184 offset:0
	ds_read_b64_tr_b16 v[36:37], v184 offset:0x200
	ds_read_b64_tr_b16 v[42:43], v184 offset:0x400
	ds_read_b64_tr_b16 v[44:45], v184 offset:0x600
	ds_read_b64_tr_b16 v[46:47], v184 offset:0x820
	ds_read_b64_tr_b16 v[48:49], v184 offset:0xa20
	ds_read_b64_tr_b16 v[102:103], v184 offset:0xc20
	ds_read_b64_tr_b16 v[104:105], v184 offset:0xe20
	ds_read_b64_tr_b16 v[106:107], v184 offset:0x1040
	ds_read_b64_tr_b16 v[108:109], v184 offset:0x1240
	ds_read_b64_tr_b16 v[110:111], v184 offset:0x1440
	ds_read_b64_tr_b16 v[112:113], v184 offset:0x1640
	s_waitcnt lgkmcnt(4)
	s_nop 0
	v_mfma_f32_16x16x32_bf16 v[2:5], v[34:37], v[82:85], v[2:5]
	v_mfma_f32_16x16x32_bf16 v[6:9], v[34:37], v[86:89], v[6:9]
	v_mfma_f32_16x16x32_bf16 v[34:37], v[46:49], v[82:85], v[38:41]
	v_mfma_f32_16x16x32_bf16 v[46:49], v[46:49], v[86:89], v[90:93]
	v_mfma_f32_16x16x32_bf16 v[38:41], v[42:45], v[94:97], v[2:5]
	v_mfma_f32_16x16x32_bf16 v[6:9], v[42:45], v[98:101], v[6:9]
	v_mfma_f32_16x16x32_bf16 v[34:37], v[102:105], v[94:97], v[34:37]
	v_mfma_f32_16x16x32_bf16 v[2:5], v[102:105], v[98:101], v[46:49]
	ds_read_b64_tr_b16 v[46:47], v184 offset:0x1860
	ds_read_b64_tr_b16 v[48:49], v184 offset:0x1a60
	ds_read_b64_tr_b16 v[90:91], v184 offset:0x1c60
	ds_read_b64_tr_b16 v[92:93], v184 offset:0x1e60
	s_waitcnt lgkmcnt(4)
	v_mfma_f32_16x16x32_bf16 v[10:13], v[106:109], v[82:85], v[10:13]
	s_waitcnt lgkmcnt(0)
	v_mfma_f32_16x16x32_bf16 v[22:25], v[106:109], v[86:89], v[22:25]
	v_mfma_f32_16x16x32_bf16 v[42:45], v[110:113], v[94:97], v[10:13]
	v_mfma_f32_16x16x32_bf16 v[10:13], v[110:113], v[98:101], v[22:25]
	v_mfma_f32_16x16x32_bf16 v[14:17], v[46:49], v[82:85], v[14:17]
	v_mfma_f32_16x16x32_bf16 v[18:21], v[46:49], v[86:89], v[18:21]
	v_mfma_f32_16x16x32_bf16 v[46:49], v[90:93], v[94:97], v[14:17]
	v_mfma_f32_16x16x32_bf16 v[14:17], v[90:93], v[98:101], v[18:21]
	s_waitcnt vmcnt(0)
	ds_read_b64_tr_b16 v[18:19], v184 offset:0x2080
	ds_read_b64_tr_b16 v[20:21], v184 offset:0x2280
	ds_read_b64_tr_b16 v[22:23], v184 offset:0x2480
	ds_read_b64_tr_b16 v[24:25], v184 offset:0x2680
	ds_read_b64_tr_b16 v[90:91], v184 offset:0x28a0
	ds_read_b64_tr_b16 v[92:93], v184 offset:0x2aa0
	ds_read_b64_tr_b16 v[102:103], v184 offset:0x2ca0
	ds_read_b64_tr_b16 v[104:105], v184 offset:0x2ea0
	ds_read_b64_tr_b16 v[106:107], v184 offset:0x30c0
	ds_read_b64_tr_b16 v[108:109], v184 offset:0x32c0
	ds_read_b64_tr_b16 v[110:111], v184 offset:0x34c0
	ds_read_b64_tr_b16 v[112:113], v184 offset:0x36c0
	s_waitcnt lgkmcnt(4)
	s_nop 5
	v_mfma_f32_16x16x32_bf16 v[50:53], v[18:21], v[82:85], v[50:53]
	v_mfma_f32_16x16x32_bf16 v[18:21], v[18:21], v[86:89], v[54:57]
	v_mfma_f32_16x16x32_bf16 v[70:73], v[90:93], v[82:85], v[70:73]
	v_mfma_f32_16x16x32_bf16 v[78:81], v[90:93], v[86:89], v[78:81]
	v_mfma_f32_16x16x32_bf16 v[54:57], v[22:25], v[94:97], v[50:53]
	v_mfma_f32_16x16x32_bf16 v[22:25], v[22:25], v[98:101], v[18:21]
	v_mfma_f32_16x16x32_bf16 v[50:53], v[102:105], v[94:97], v[70:73]
	v_mfma_f32_16x16x32_bf16 v[18:21], v[102:105], v[98:101], v[78:81]
	ds_read_b64_tr_b16 v[70:71], v184 offset:0x38e0
	ds_read_b64_tr_b16 v[72:73], v184 offset:0x3ae0
	ds_read_b64_tr_b16 v[78:79], v184 offset:0x3ce0
	ds_read_b64_tr_b16 v[80:81], v184 offset:0x3ee0
	s_waitcnt lgkmcnt(4)
	v_mfma_f32_16x16x32_bf16 v[26:29], v[106:109], v[82:85], v[26:29]
	s_waitcnt lgkmcnt(0)
	v_mfma_f32_16x16x32_bf16 v[90:93], v[106:109], v[86:89], v[58:61]
	v_mfma_f32_16x16x32_bf16 v[58:61], v[110:113], v[94:97], v[26:29]
	v_mfma_f32_16x16x32_bf16 v[26:29], v[110:113], v[98:101], v[90:93]
	v_mfma_f32_16x16x32_bf16 v[30:33], v[70:73], v[82:85], v[30:33]
	v_mfma_f32_16x16x32_bf16 v[70:73], v[70:73], v[86:89], v[62:65]
	v_mfma_f32_16x16x32_bf16 v[62:65], v[78:81], v[94:97], v[30:33]
	v_mfma_f32_16x16x32_bf16 v[30:33], v[78:81], v[98:101], v[70:73]
	v_add_f32_e64 v66, v66, v68
	v_add_f32_e64 v67, v67, v69
	v_pk_add_f32 v[68:69], v[114:115], v[114:115] op_sel:[0,1] op_sel_hi:[1,0]
	v_pk_add_f32 v[66:67], v[66:67], v[66:67] op_sel:[0,1] op_sel_hi:[1,0]
	v_add_f32_e32 v74, v116, v117
	v_add_f32_e32 v76, v118, v119
	v_mov_b32_e32 v69, v120
	v_mov_b32_e32 v67, v121
	v_pk_add_f32 v[66:67], v[68:69], v[66:67]
	v_pk_add_f32 v[68:69], v[74:75], v[76:77]
	s_nop 0
	v_pk_add_f32 v[66:67], v[66:67], v[68:69]
	s_nop 0
	v_add_f32_e32 v66, v66, v67
	s_setprio 0
	ds_bpermute_b32 v67, v177, v66
	ds_bpermute_b32 v68, v177, v122
	v_mov_b32_e32 v70, v185
	s_waitcnt lgkmcnt(1)
	v_add_f32_e32 v66, v66, v67
	s_waitcnt lgkmcnt(0)
	v_add_f32_e32 v67, v122, v68
	ds_bpermute_b32 v68, v188, v66
	ds_bpermute_b32 v69, v188, v67
	s_waitcnt lgkmcnt(1)
	v_add_f32_e32 v66, v66, v68
	s_waitcnt lgkmcnt(0)
	v_add_f32_e32 v67, v67, v69
	v_rcp_f32_e32 v68, v66
	v_rcp_f32_e32 v66, v67
	v_mov_b32_e32 v67, v176
	v_mov_b32_e32 v69, v180
	s_branch .LBB0_641

; __device__ __forceinline__ unsigned xb_ld(unsigned* p)              { return __hip_atomic_load(p, __ATOMIC_RELAXED, __HIP_MEMORY_SCOPE_AGENT); }
; __device__ __forceinline__ void xcd_barrier_complete(unsigned* bar, unsigned x, unsigned& nloc, unsigned& nx) {
;     const unsigned G = gridDim.x * gridDim.y * gridDim.z;
;     unsigned sum, cnt, mine, sp = 0u;
;     for (;;) {
;         sum = 0u; cnt = 0u; mine = 0u;
; #pragma unroll
;         for (unsigned j = 0; j < 16; ++j) { const unsigned c = xb_ld(&bar[XB_XCNT(j)]); sum += c; cnt += (c > 0u) ? 1u : 0u; mine = (j == x) ? c : mine; }
;         if (sum == G) break;
;         __builtin_amdgcn_s_sleep(1);
;         if ((++sp & 255u) == 0u) { if (xb_ld(&bar[XB_TMO])) break; if (sp > XB_SPIN_CAP) { atomicAdd(&bar[XB_TMO], 1u); break; } }
;     }
;     nloc = mine > 0u ? mine : 1u; nx = cnt > 0u ? cnt : 1u;
; __device__ __forceinline__ void xcd_barrier(const XcdBarrier& b) {
;     asm volatile("s_waitcnt vmcnt(0)" ::: "memory");
;     __syncthreads();
;     if (threadIdx.x == 0) {
;         unsigned* bar = b.bar;
;         __builtin_amdgcn_s_waitcnt(0);
;         unsigned nloc = b.st[0], nx = b.st[1];
;         if (nloc == 0u) { xcd_barrier_complete(bar, b.x, nloc, nx); b.st[0] = nloc; b.st[1] = nx; }
.LBB0_653:
	s_nop 0
	s_nop 0
	s_cmp_gt_i32 s81, 8
	s_cselect_b64 s[4:5], -1, 0
	s_and_b64 s[0:1], s[10:11], s[4:5]
	s_andn2_b64 vcc, exec, s[0:1]
	s_cbranch_vccnz .LBB0_707
	s_mov_b64 s[8:9], s[96:97]
	s_getreg_b32 s0, hwreg(HW_REG_XCC_ID, 0, 4)
	s_waitcnt vmcnt(0)
	s_waitcnt vmcnt(0)
	s_barrier
	s_mov_b64 s[6:7], exec
	v_readlane_b32 s2, v255, 0
	v_readlane_b32 s3, v255, 1
	s_and_b64 s[2:3], s[6:7], s[2:3]
	s_mov_b64 exec, s[2:3]
	s_cbranch_execz .LBB0_706
	s_add_i32 s1, 0, 0x22160
	v_mov_b32_e32 v2, s1
	s_load_dwordx2 s[8:9], s[8:9], 0xe8
	s_waitcnt vmcnt(0) expcnt(0) lgkmcnt(0)
	ds_read_b32 v4, v2
	s_add_i32 s1, 0, 0x22164
	v_mov_b32_e32 v2, s1
	ds_read_b32 v2, v2
	s_and_b32 s0, s0, 15
	s_waitcnt lgkmcnt(1)
	v_cmp_ne_u32_e32 vcc, 0, v4
	s_cbranch_vccnz .LBB0_670
	s_add_u32 s10, s8, 0x4200
	s_addc_u32 s11, s9, 0
	s_add_u32 s12, s8, 0x4400
	s_addc_u32 s13, s9, 0
	s_add_u32 s14, s8, 0x4500
	s_addc_u32 s15, s9, 0
	s_add_u32 s16, s8, 0x4600
	s_addc_u32 s17, s9, 0
	s_add_u32 s18, s8, 0x4700
	s_addc_u32 s19, s9, 0
	s_add_u32 s20, s8, 0x4800
	s_addc_u32 s21, s9, 0
	s_add_u32 s22, s8, 0x4900
	s_addc_u32 s23, s9, 0
	s_add_u32 s24, s8, 0x4a00
	s_addc_u32 s25, s9, 0
	s_add_u32 s26, s8, 0x4b00
	s_addc_u32 s27, s9, 0
	s_add_u32 s28, s8, 0x4c00
	s_addc_u32 s29, s9, 0
	s_add_u32 s30, s8, 0x4d00
	s_addc_u32 s31, s9, 0
	s_add_u32 s34, s8, 0x4e00
	s_addc_u32 s35, s9, 0
	s_add_u32 s36, s8, 0x4f00
	s_addc_u32 s37, s9, 0
	s_add_u32 s38, s8, 0x5000
	s_addc_u32 s39, s9, 0
	s_load_dwordx2 s[2:3], s[96:97], 0xf8
	s_load_dword s1, s[96:97], 0x100
	s_add_u32 s40, s8, 0x5100
	s_addc_u32 s41, s9, 0
	s_add_u32 s42, s8, 0x5200
	s_addc_u32 s43, s9, 0
	s_waitcnt lgkmcnt(0)
	s_mul_i32 s2, s3, s2
	s_add_u32 s44, s8, 0x5300
	s_mul_i32 s1, s2, s1
	s_addc_u32 s45, s9, 0
	s_mov_b32 s2, 1
	v_mov_b32_e32 v18, 0
	s_branch .LBB0_658

; #define SBAR() __builtin_amdgcn_sched_barrier(0)
; #define ELOADV(kt) do { const char* vb_ = (const char*)Vh + (size_t)(kt) * (64 * LDV * 2); sv0 = *(const bf16x8*)(vb_ + voff0); sv1 = *(const bf16x8*)(vb_ + voff1); sv2 = *(const bf16x8*)(vb_ + voff0 + 256); sv3 = *(const bf16x8*)(vb_ + voff1 + 256); } while (0)
; #define ELOADK(kt) do { const char* kb_ = (const char*)Kh + (size_t)(kt) * (64 * LDK * 2); sk0 = *(const bf16x8*)(kb_ + koff0); sk1 = *(const bf16x8*)(kb_ + koff1); } while (0)
; #define EWRITEV(b) do { char* d_ = V_lds + (b) * D16_V; *(bf16x8*)(d_ + vst0) = sv0; *(bf16x8*)(d_ + vst1) = sv1; *(bf16x8*)(d_ + 8 * VP16 + vst0) = sv2; *(bf16x8*)(d_ + 8 * VP16 + vst1) = sv3; } while (0)
; #define EWRITEK(b) do { char* d_ = K_lds + (b) * PB_K; *(bf16x8*)(d_ + KSWZ(sr, sc * 2)) = sk0; *(bf16x8*)(d_ + KSWZ(32 + sr, sc * 2)) = sk1; } while (0)
; template <int LDQ, int LDK, int LDV, int LDO, int DMX> ...
;     ...
;     asm volatile("s_waitcnt vmcnt(0)" ::: "memory");
;     if (t + 2 < NT) EWRITEK(t & 1);
;     if (t + 1 < NT) EWRITEV((t + 1) & 1);
;     ELOADK(t + 3); ELOADV(t + 2);
;     SBAR(); pv16d<4>(o, vbo, vbp, pc, pp); SBAR();
;     if (more) ESM((t + 1) & 1);
.Lvd_kskip:
	v_lshl_add_u64 v[240:241], v[176:177], 0, s[6:7]
	v_add_co_u32_e32 v242, vcc, s41, v240
	s_nop 1
	v_addc_co_u32_e32 v243, vcc, 0, v241, vcc
	v_add_co_u32_e32 v240, vcc, s42, v240
	s_nop 1
	v_addc_co_u32_e32 v241, vcc, 0, v241, vcc
	global_load_dwordx4 v[52:55], v[242:243], off offset:1024
	global_load_dwordx4 v[56:59], v[240:241], off offset:1024
	s_waitcnt lgkmcnt(4)
	s_nop 0
	v_mfma_f32_16x16x32_bf16 v[84:87], v[36:39], v[64:67], v[84:87]
	v_exp_f32_e32 v144, v144
	v_mfma_f32_16x16x32_bf16 v[92:95], v[36:39], v[68:71], v[92:95]
	v_exp_f32_e32 v240, v145
	v_mfma_f32_16x16x32_bf16 v[88:91], v[44:47], v[64:67], v[88:91]
	v_exp_f32_e32 v146, v146
	v_mfma_f32_16x16x32_bf16 v[96:99], v[44:47], v[68:71], v[96:99]
	v_exp_f32_e32 v242, v147
	v_mfma_f32_16x16x32_bf16 v[84:87], v[40:43], v[148:151], v[84:87]
	v_exp_f32_e32 v145, v140
	v_mfma_f32_16x16x32_bf16 v[92:95], v[40:43], v[152:155], v[92:95]
	v_exp_f32_e32 v241, v141
	v_mfma_f32_16x16x32_bf16 v[88:91], v[48:51], v[148:151], v[88:91]
	v_exp_f32_e32 v147, v142
	v_mfma_f32_16x16x32_bf16 v[96:99], v[48:51], v[152:155], v[96:99]
	v_exp_f32_e32 v243, v143
	ds_read_b64_tr_b16 v[180:181], v179 offset:0x38e0
	ds_read_b64_tr_b16 v[182:183], v179 offset:0x3ae0
	ds_read_b64_tr_b16 v[204:205], v178 offset:0x38e0
	ds_read_b64_tr_b16 v[206:207], v178 offset:0x3ae0
	s_waitcnt lgkmcnt(4)
	v_mfma_f32_16x16x32_bf16 v[60:63], v[232:235], v[64:67], v[60:63]
	v_exp_f32_e32 v136, v136
	s_waitcnt lgkmcnt(0)
	v_mfma_f32_16x16x32_bf16 v[80:83], v[232:235], v[68:71], v[80:83]
	v_exp_f32_e32 v140, v137
	v_mfma_f32_16x16x32_bf16 v[60:63], v[236:239], v[148:151], v[60:63]
	v_exp_f32_e32 v138, v138
	v_mfma_f32_16x16x32_bf16 v[80:83], v[236:239], v[152:155], v[80:83]
	v_exp_f32_e32 v142, v139
	v_mfma_f32_16x16x32_bf16 v[64:67], v[180:183], v[64:67], v[72:75]
	v_exp_f32_e32 v137, v132
	v_mfma_f32_16x16x32_bf16 v[68:71], v[180:183], v[68:71], v[76:79]
	v_exp_f32_e32 v141, v133
	v_mfma_f32_16x16x32_bf16 v[72:75], v[204:207], v[148:151], v[64:67]
	v_exp_f32_e32 v139, v134
	v_mfma_f32_16x16x32_bf16 v[76:79], v[204:207], v[152:155], v[68:71]
	v_exp_f32_e32 v143, v135
	s_nop 4
	s_and_b32 s22, s56, 0x4000
	v_add_u32_e32 v132, s22, v190
	v_cvt_pk_bf16_f32 v64, v144, v240
	v_cvt_pk_bf16_f32 v65, v146, v242
	v_cvt_pk_bf16_f32 v66, v136, v140
	v_cvt_pk_bf16_f32 v67, v138, v142
	v_cvt_pk_bf16_f32 v68, v145, v241
	v_cvt_pk_bf16_f32 v69, v147, v243
	v_cvt_pk_bf16_f32 v70, v137, v141
	v_cvt_pk_bf16_f32 v71, v139, v143
	ds_write_b128 v132, v[64:67]
	ds_write_b128 v132, v[68:71] offset:1024
	v_pk_add_f32 v[132:133], v[144:145], v[240:241]
	v_pk_add_f32 v[134:135], v[146:147], v[242:243]
	s_add_u32 s6, s6, 0xc0000
	v_pk_add_f32 v[132:133], v[132:133], v[134:135]
	v_pk_add_f32 v[134:135], v[136:137], v[140:141]
	v_pk_add_f32 v[136:137], v[138:139], v[142:143]
	s_addc_u32 s7, s7, 0
	v_pk_add_f32 v[134:135], v[134:135], v[136:137]
	s_add_i32 s55, s55, 1
	v_pk_add_f32 v[132:133], v[132:133], v[134:135]
	s_addk_i32 s56, 0x4000
	s_cmp_eq_u32 s6, 0xc240000
	v_pk_add_f32 v[174:175], v[174:175], v[132:133]
	s_cbranch_scc0 .LBB0_1271
